# grid barrier: the last cross-XCC arriver releases the workgroups of every XCC directly (adds on all 16 per-XCC generation words) instead of releasing leaders that then release their XCC; leaders no lo
# speedup vs baseline: 1.0066x; 1.0054x over previous
.LBB0_58:
	s_or_b64 exec, exec, s[14:15]
	v_cvt_f32_u32_e32 v4, v1
	s_waitcnt vmcnt(0)
	v_readfirstlane_b32 s0, v3
	s_add_u32 s14, s8, 0x3500
	s_addc_u32 s15, s9, 0
	v_rcp_iflag_f32_e32 v4, v4
	v_add_u32_e32 v2, s0, v2
	v_add_u32_e32 v5, 1, v2
	s_mov_b64 s[16:17], -1
	v_mul_f32_e32 v3, 0x4f7ffffe, v4
	v_cvt_u32_f32_e32 v3, v3
	v_sub_u32_e32 v4, 0, v1
	v_mul_lo_u32 v4, v4, v3
	v_mul_hi_u32 v4, v3, v4
	v_add_u32_e32 v3, v3, v4
	v_mul_hi_u32 v3, v2, v3
	v_mul_lo_u32 v4, v3, v1
	v_sub_u32_e32 v2, v2, v4
	v_add_u32_e32 v6, 1, v3
	v_cmp_ge_u32_e32 vcc, v2, v1
	v_sub_u32_e32 v4, v2, v1
	s_nop 0
	v_cndmask_b32_e32 v3, v3, v6, vcc
	v_cndmask_b32_e32 v2, v2, v4, vcc
	v_add_u32_e32 v4, 1, v3
	v_cmp_ge_u32_e32 vcc, v2, v1
	s_nop 1
	v_cndmask_b32_e32 v4, v3, v4, vcc
	v_mul_lo_u32 v2, v1, v4
	v_add_u32_e32 v1, v2, v1
	v_cmp_ne_u32_e32 vcc, v5, v1
	v_mov_b64_e32 v[2:3], s[14:15]
	s_cbranch_vccnz .Lmy_gs0
	v_mov_b32_e32 v5, 0x2400
	v_mov_b32_e32 v1, 1
	global_atomic_add v5, v1, s[8:9]
	global_atomic_add v5, v1, s[8:9] offset:256
	global_atomic_add v5, v1, s[8:9] offset:512
	global_atomic_add v5, v1, s[8:9] offset:768
	global_atomic_add v5, v1, s[8:9] offset:1024
	global_atomic_add v5, v1, s[8:9] offset:1280
	global_atomic_add v5, v1, s[8:9] offset:1536
	global_atomic_add v5, v1, s[8:9] offset:1792
	global_atomic_add v5, v1, s[8:9] offset:2048
	global_atomic_add v5, v1, s[8:9] offset:2304
	global_atomic_add v5, v1, s[8:9] offset:2560
	global_atomic_add v5, v1, s[8:9] offset:2816
	global_atomic_add v5, v1, s[8:9] offset:3072
	global_atomic_add v5, v1, s[8:9] offset:3328
	global_atomic_add v5, v1, s[8:9] offset:3584
	global_atomic_add v5, v1, s[8:9] offset:3840
.Lmy_gs0:
	s_and_saveexec_b64 s[12:13], vcc
	s_cbranch_execz .LBB0_70
	v_mov_b32_e32 v1, 0
	global_load_dword v2, v1, s[14:15] sc1
	s_mov_b64 s[20:21], 0
	s_waitcnt vmcnt(0)
	v_cmp_eq_u32_e32 vcc, v2, v4
	s_and_saveexec_b64 s[18:19], vcc
	s_cbranch_execz .LBB0_69
	s_add_u32 s16, s8, 0x200
	s_addc_u32 s17, s9, 0
	s_mov_b32 s0, 1
	s_mov_b64 s[8:9], 0
	s_branch .LBB0_62

.LBB0_72:
	s_or_b64 exec, exec, s[8:9]
	s_mov_b64 s[8:9], exec
	v_mbcnt_lo_u32_b32 v1, s8, 0
	v_mbcnt_hi_u32_b32 v1, s9, v1
	v_cmp_eq_u32_e32 vcc, 0, v1
	s_waitcnt vmcnt(0)
	buffer_inv sc1
	s_and_saveexec_b64 s[12:13], vcc
	s_cbranch_execz .LBB0_74
	s_bcnt1_i32_b64 s0, s[8:9]
	v_mov_b32_e32 v1, 0x2000
	v_mov_b32_e32 v2, s0
.LBB0_74:
	s_or_b64 exec, exec, s[12:13]
	s_waitcnt vmcnt(0)

.LBB0_181:
	s_or_b64 exec, exec, s[8:9]
	s_mov_b64 s[8:9], exec
	v_mbcnt_lo_u32_b32 v1, s8, 0
	v_mbcnt_hi_u32_b32 v1, s9, v1
	v_cmp_eq_u32_e32 vcc, 0, v1
	s_waitcnt vmcnt(0)
	buffer_inv sc1
	s_and_saveexec_b64 s[12:13], vcc
	s_cbranch_execz .LBB0_183
	s_bcnt1_i32_b64 s0, s[8:9]
	v_mov_b32_e32 v1, 0x2000
	v_mov_b32_e32 v2, s0
.LBB0_183:
	s_or_b64 exec, exec, s[12:13]
	s_waitcnt vmcnt(0)

.LBB0_254:
	s_or_b64 exec, exec, s[8:9]
	s_mov_b64 s[8:9], exec
	v_mbcnt_lo_u32_b32 v1, s8, 0
	v_mbcnt_hi_u32_b32 v1, s9, v1
	v_cmp_eq_u32_e32 vcc, 0, v1
	s_waitcnt vmcnt(0)
	buffer_inv sc1
	s_and_saveexec_b64 s[12:13], vcc
	s_cbranch_execz .LBB0_256
	s_bcnt1_i32_b64 s0, s[8:9]
	v_mov_b32_e32 v1, 0x2000
	v_mov_b32_e32 v2, s0
.LBB0_256:
	s_or_b64 exec, exec, s[12:13]
	s_waitcnt vmcnt(0)

.LBB0_354:
	s_or_b64 exec, exec, s[8:9]
	s_mov_b64 s[8:9], exec
	v_mbcnt_lo_u32_b32 v1, s8, 0
	v_mbcnt_hi_u32_b32 v1, s9, v1
	v_cmp_eq_u32_e32 vcc, 0, v1
	s_waitcnt vmcnt(0)
	buffer_inv sc1
	s_and_saveexec_b64 s[12:13], vcc
	s_cbranch_execz .LBB0_356
	s_bcnt1_i32_b64 s0, s[8:9]
	v_mov_b32_e32 v1, 0x2000
	v_mov_b32_e32 v2, s0
.LBB0_356:
	s_or_b64 exec, exec, s[12:13]
	s_waitcnt vmcnt(0)

.LBB0_618:
	s_or_b64 exec, exec, s[8:9]
	s_mov_b64 s[8:9], exec
	v_mbcnt_lo_u32_b32 v1, s8, 0
	v_mbcnt_hi_u32_b32 v1, s9, v1
	v_cmp_eq_u32_e32 vcc, 0, v1
	s_waitcnt vmcnt(0)
	buffer_inv sc1
	s_and_saveexec_b64 s[12:13], vcc
	s_cbranch_execz .LBB0_620
	s_bcnt1_i32_b64 s0, s[8:9]
	v_mov_b32_e32 v1, 0x2000
	v_mov_b32_e32 v2, s0
.LBB0_620:
	s_or_b64 exec, exec, s[12:13]
	s_waitcnt vmcnt(0)

.LBB0_943:
	s_or_b64 exec, exec, s[8:9]
	s_mov_b64 s[8:9], exec
	v_mbcnt_lo_u32_b32 v1, s8, 0
	v_mbcnt_hi_u32_b32 v1, s9, v1
	v_cmp_eq_u32_e32 vcc, 0, v1
	s_waitcnt vmcnt(0)
	buffer_inv sc1
	s_and_saveexec_b64 s[12:13], vcc
	s_cbranch_execz .LBB0_945
	s_bcnt1_i32_b64 s0, s[8:9]
	v_mov_b32_e32 v1, 0x2000
	v_mov_b32_e32 v2, s0
.LBB0_945:
	s_or_b64 exec, exec, s[12:13]
	s_waitcnt vmcnt(0)

.LBB0_1017:
	s_or_b64 exec, exec, s[8:9]
	s_mov_b64 s[8:9], exec
	v_mbcnt_lo_u32_b32 v1, s8, 0
	v_mbcnt_hi_u32_b32 v1, s9, v1
	v_cmp_eq_u32_e32 vcc, 0, v1
	s_waitcnt vmcnt(0)
	buffer_inv sc1
	s_and_saveexec_b64 s[12:13], vcc
	s_cbranch_execz .LBB0_1019
	s_bcnt1_i32_b64 s0, s[8:9]
	v_mov_b32_e32 v1, 0x2000
	v_mov_b32_e32 v2, s0
.LBB0_1019:
	s_or_b64 exec, exec, s[12:13]
	s_waitcnt vmcnt(0)

.LBB0_1358:
	s_or_b64 exec, exec, s[16:17]
	v_cvt_f32_u32_e32 v4, v1
	s_waitcnt vmcnt(0)
	v_readfirstlane_b32 s0, v3
	s_add_u32 s16, s10, 0x3500
	s_addc_u32 s17, s11, 0
	v_rcp_iflag_f32_e32 v4, v4
	v_add_u32_e32 v2, s0, v2
	v_add_u32_e32 v5, 1, v2
	s_mov_b64 s[18:19], -1
	v_mul_f32_e32 v3, 0x4f7ffffe, v4
	v_cvt_u32_f32_e32 v3, v3
	v_sub_u32_e32 v4, 0, v1
	v_mul_lo_u32 v4, v4, v3
	v_mul_hi_u32 v4, v3, v4
	v_add_u32_e32 v3, v3, v4
	v_mul_hi_u32 v3, v2, v3
	v_mul_lo_u32 v4, v3, v1
	v_sub_u32_e32 v2, v2, v4
	v_add_u32_e32 v6, 1, v3
	v_cmp_ge_u32_e32 vcc, v2, v1
	v_sub_u32_e32 v4, v2, v1
	s_nop 0
	v_cndmask_b32_e32 v3, v3, v6, vcc
	v_cndmask_b32_e32 v2, v2, v4, vcc
	v_add_u32_e32 v4, 1, v3
	v_cmp_ge_u32_e32 vcc, v2, v1
	s_nop 1
	v_cndmask_b32_e32 v4, v3, v4, vcc
	v_mul_lo_u32 v2, v1, v4
	v_add_u32_e32 v1, v2, v1
	v_cmp_ne_u32_e32 vcc, v5, v1
	v_mov_b64_e32 v[2:3], s[16:17]
	s_cbranch_vccnz .Lmy_gs7
	v_mov_b32_e32 v5, 0x2400
	v_mov_b32_e32 v1, 1
	global_atomic_add v5, v1, s[10:11]
	global_atomic_add v5, v1, s[10:11] offset:256
	global_atomic_add v5, v1, s[10:11] offset:512
	global_atomic_add v5, v1, s[10:11] offset:768
	global_atomic_add v5, v1, s[10:11] offset:1024
	global_atomic_add v5, v1, s[10:11] offset:1280
	global_atomic_add v5, v1, s[10:11] offset:1536
	global_atomic_add v5, v1, s[10:11] offset:1792
	global_atomic_add v5, v1, s[10:11] offset:2048
	global_atomic_add v5, v1, s[10:11] offset:2304
	global_atomic_add v5, v1, s[10:11] offset:2560
	global_atomic_add v5, v1, s[10:11] offset:2816
	global_atomic_add v5, v1, s[10:11] offset:3072
	global_atomic_add v5, v1, s[10:11] offset:3328
	global_atomic_add v5, v1, s[10:11] offset:3584
	global_atomic_add v5, v1, s[10:11] offset:3840
.Lmy_gs7:
	s_and_saveexec_b64 s[14:15], vcc
	s_cbranch_execz .LBB0_1370
	v_mov_b32_e32 v1, 0
	global_load_dword v2, v1, s[16:17] sc1
	s_mov_b64 s[22:23], 0
	s_waitcnt vmcnt(0)
	v_cmp_eq_u32_e32 vcc, v2, v4
	s_and_saveexec_b64 s[20:21], vcc
	s_cbranch_execz .LBB0_1369
	s_add_u32 s18, s10, 0x200
	s_addc_u32 s19, s11, 0
	s_mov_b32 s0, 1
	s_mov_b64 s[10:11], 0
	s_branch .LBB0_1362

.LBB0_1372:
	s_or_b64 exec, exec, s[10:11]
	s_mov_b64 s[10:11], exec
	v_mbcnt_lo_u32_b32 v1, s10, 0
	v_mbcnt_hi_u32_b32 v1, s11, v1
	v_cmp_eq_u32_e32 vcc, 0, v1
	s_waitcnt vmcnt(0)
	buffer_inv sc1
	s_and_saveexec_b64 s[14:15], vcc
	s_cbranch_execz .LBB0_1374
	s_bcnt1_i32_b64 s0, s[10:11]
	v_mov_b32_e32 v1, 0x2000
	v_mov_b32_e32 v2, s0
.LBB0_1374:
	s_or_b64 exec, exec, s[14:15]
	s_waitcnt vmcnt(0)

.LBB0_1463:
	s_or_b64 exec, exec, s[8:9]
	s_mov_b64 s[8:9], exec
	v_mbcnt_lo_u32_b32 v1, s8, 0
	v_mbcnt_hi_u32_b32 v1, s9, v1
	v_cmp_eq_u32_e32 vcc, 0, v1
	s_waitcnt vmcnt(0)
	buffer_inv sc1
	s_and_saveexec_b64 s[12:13], vcc
	s_cbranch_execz .LBB0_1465
	s_bcnt1_i32_b64 s0, s[8:9]
	v_mov_b32_e32 v1, 0x2000
	v_mov_b32_e32 v2, s0
.LBB0_1465:
	s_or_b64 exec, exec, s[12:13]
	s_waitcnt vmcnt(0)

.LBB0_1593:
	s_or_b64 exec, exec, s[18:19]
	v_cvt_f32_u32_e32 v4, v1
	s_waitcnt vmcnt(0)
	v_readfirstlane_b32 s16, v3
	s_add_u32 s18, s12, 0x3500
	s_addc_u32 s19, s13, 0
	v_rcp_iflag_f32_e32 v4, v4
	v_add_u32_e32 v2, s16, v2
	v_add_u32_e32 v5, 1, v2
	s_mov_b64 s[22:23], -1
	v_mul_f32_e32 v3, 0x4f7ffffe, v4
	v_cvt_u32_f32_e32 v3, v3
	v_sub_u32_e32 v4, 0, v1
	v_mul_lo_u32 v4, v4, v3
	v_mul_hi_u32 v4, v3, v4
	v_add_u32_e32 v3, v3, v4
	v_mul_hi_u32 v3, v2, v3
	v_mul_lo_u32 v4, v3, v1
	v_sub_u32_e32 v2, v2, v4
	v_add_u32_e32 v6, 1, v3
	v_cmp_ge_u32_e32 vcc, v2, v1
	v_sub_u32_e32 v4, v2, v1
	s_nop 0
	v_cndmask_b32_e32 v3, v3, v6, vcc
	v_cndmask_b32_e32 v2, v2, v4, vcc
	v_add_u32_e32 v4, 1, v3
	v_cmp_ge_u32_e32 vcc, v2, v1
	s_nop 1
	v_cndmask_b32_e32 v4, v3, v4, vcc
	v_mul_lo_u32 v2, v1, v4
	v_add_u32_e32 v1, v2, v1
	v_cmp_ne_u32_e32 vcc, v5, v1
	v_mov_b64_e32 v[2:3], s[18:19]
	s_cbranch_vccnz .Lmy_gs9
	v_mov_b32_e32 v5, 0x2400
	v_mov_b32_e32 v1, 1
	global_atomic_add v5, v1, s[12:13]
	global_atomic_add v5, v1, s[12:13] offset:256
	global_atomic_add v5, v1, s[12:13] offset:512
	global_atomic_add v5, v1, s[12:13] offset:768
	global_atomic_add v5, v1, s[12:13] offset:1024
	global_atomic_add v5, v1, s[12:13] offset:1280
	global_atomic_add v5, v1, s[12:13] offset:1536
	global_atomic_add v5, v1, s[12:13] offset:1792
	global_atomic_add v5, v1, s[12:13] offset:2048
	global_atomic_add v5, v1, s[12:13] offset:2304
	global_atomic_add v5, v1, s[12:13] offset:2560
	global_atomic_add v5, v1, s[12:13] offset:2816
	global_atomic_add v5, v1, s[12:13] offset:3072
	global_atomic_add v5, v1, s[12:13] offset:3328
	global_atomic_add v5, v1, s[12:13] offset:3584
	global_atomic_add v5, v1, s[12:13] offset:3840
.Lmy_gs9:
	s_and_saveexec_b64 s[16:17], vcc
	s_cbranch_execz .LBB0_1605
	v_mov_b32_e32 v1, 0
	global_load_dword v2, v1, s[18:19] sc1
	s_mov_b64 s[26:27], 0
	s_waitcnt vmcnt(0)
	v_cmp_eq_u32_e32 vcc, v2, v4
	s_and_saveexec_b64 s[24:25], vcc
	s_cbranch_execz .LBB0_1604
	s_add_u32 s22, s12, 0x200
	s_addc_u32 s23, s13, 0
	s_mov_b32 s33, 1
	s_mov_b64 s[12:13], 0
	s_branch .LBB0_1597

.LBB0_1607:
	s_or_b64 exec, exec, s[12:13]
	s_mov_b64 s[12:13], exec
	v_mbcnt_lo_u32_b32 v1, s12, 0
	v_mbcnt_hi_u32_b32 v1, s13, v1
	v_cmp_eq_u32_e32 vcc, 0, v1
	s_waitcnt vmcnt(0)
	buffer_inv sc1
	s_and_saveexec_b64 s[16:17], vcc
	s_cbranch_execz .LBB0_1609
	s_bcnt1_i32_b64 s12, s[12:13]
	v_mov_b32_e32 v1, 0x2000
	v_mov_b32_e32 v2, s12
.LBB0_1609:
	s_or_b64 exec, exec, s[16:17]
	s_waitcnt vmcnt(0)

.LBB0_1715:
	s_or_b64 exec, exec, s[12:13]
	v_cvt_f32_u32_e32 v4, v1
	s_waitcnt vmcnt(0)
	v_readfirstlane_b32 s0, v3
	s_add_u32 s12, s4, 0x3500
	s_addc_u32 s13, s5, 0
	v_rcp_iflag_f32_e32 v4, v4
	v_add_u32_e32 v2, s0, v2
	v_add_u32_e32 v5, 1, v2
	s_mov_b64 s[14:15], -1
	v_mul_f32_e32 v3, 0x4f7ffffe, v4
	v_cvt_u32_f32_e32 v3, v3
	v_sub_u32_e32 v4, 0, v1
	v_mul_lo_u32 v4, v4, v3
	v_mul_hi_u32 v4, v3, v4
	v_add_u32_e32 v3, v3, v4
	v_mul_hi_u32 v3, v2, v3
	v_mul_lo_u32 v4, v3, v1
	v_sub_u32_e32 v2, v2, v4
	v_add_u32_e32 v6, 1, v3
	v_cmp_ge_u32_e32 vcc, v2, v1
	v_sub_u32_e32 v4, v2, v1
	s_nop 0
	v_cndmask_b32_e32 v3, v3, v6, vcc
	v_cndmask_b32_e32 v2, v2, v4, vcc
	v_add_u32_e32 v4, 1, v3
	v_cmp_ge_u32_e32 vcc, v2, v1
	s_nop 1
	v_cndmask_b32_e32 v4, v3, v4, vcc
	v_mul_lo_u32 v2, v1, v4
	v_add_u32_e32 v1, v2, v1
	v_cmp_ne_u32_e32 vcc, v5, v1
	v_mov_b64_e32 v[2:3], s[12:13]
	s_cbranch_vccnz .Lmy_gs10
	v_mov_b32_e32 v5, 0x2400
	v_mov_b32_e32 v1, 1
	global_atomic_add v5, v1, s[4:5]
	global_atomic_add v5, v1, s[4:5] offset:256
	global_atomic_add v5, v1, s[4:5] offset:512
	global_atomic_add v5, v1, s[4:5] offset:768
	global_atomic_add v5, v1, s[4:5] offset:1024
	global_atomic_add v5, v1, s[4:5] offset:1280
	global_atomic_add v5, v1, s[4:5] offset:1536
	global_atomic_add v5, v1, s[4:5] offset:1792
	global_atomic_add v5, v1, s[4:5] offset:2048
	global_atomic_add v5, v1, s[4:5] offset:2304
	global_atomic_add v5, v1, s[4:5] offset:2560
	global_atomic_add v5, v1, s[4:5] offset:2816
	global_atomic_add v5, v1, s[4:5] offset:3072
	global_atomic_add v5, v1, s[4:5] offset:3328
	global_atomic_add v5, v1, s[4:5] offset:3584
	global_atomic_add v5, v1, s[4:5] offset:3840
.Lmy_gs10:
	s_and_saveexec_b64 s[10:11], vcc
	s_cbranch_execz .LBB0_1727
	v_mov_b32_e32 v1, 0
	global_load_dword v2, v1, s[12:13] sc1
	s_mov_b64 s[18:19], 0
	s_waitcnt vmcnt(0)
	v_cmp_eq_u32_e32 vcc, v2, v4
	s_and_saveexec_b64 s[16:17], vcc
	s_cbranch_execz .LBB0_1726
	s_add_u32 s14, s4, 0x200
	s_addc_u32 s15, s5, 0
	s_mov_b32 s0, 1
	s_mov_b64 s[4:5], 0
	s_branch .LBB0_1719

.LBB0_1729:
	s_or_b64 exec, exec, s[4:5]
	s_mov_b64 s[4:5], exec
	v_mbcnt_lo_u32_b32 v1, s4, 0
	v_mbcnt_hi_u32_b32 v1, s5, v1
	v_cmp_eq_u32_e32 vcc, 0, v1
	s_waitcnt vmcnt(0)
	buffer_inv sc1
	s_and_saveexec_b64 s[10:11], vcc
	s_cbranch_execz .LBB0_1731
	s_bcnt1_i32_b64 s0, s[4:5]
	v_mov_b32_e32 v1, 0x2000
	v_mov_b32_e32 v2, s0
.LBB0_1731:
	s_or_b64 exec, exec, s[10:11]
	s_waitcnt vmcnt(0)
